# conformer conv ladder: per-tap FMAs paired into v_pk_fma_f32 (same operands, fused), weights copied once into a parity-shifted register set
# speedup vs baseline: 1.0067x; 1.0026x over previous
.LBB0_2163:
	s_or_b64 exec, exec, s[18:19]
	v_readlane_b32 s36, v251, 19
	v_readlane_b32 s50, v251, 33
	v_readlane_b32 s37, v251, 20
	v_readlane_b32 s38, v251, 21
	v_readlane_b32 s39, v251, 22
	v_readlane_b32 s40, v251, 23
	v_readlane_b32 s41, v251, 24
	v_readlane_b32 s42, v251, 25
	v_readlane_b32 s43, v251, 26
	v_readlane_b32 s44, v251, 27
	v_readlane_b32 s45, v251, 28
	v_readlane_b32 s46, v251, 29
	v_readlane_b32 s47, v251, 30
	v_readlane_b32 s48, v251, 31
	v_readlane_b32 s49, v251, 32
	v_readlane_b32 s51, v251, 34
	s_add_u32 s18, s50, s16
	s_addc_u32 s19, s51, s17
	v_readlane_b32 s36, v251, 35
	v_readlane_b32 s37, v251, 36
	s_add_u32 s16, s36, s16
	s_waitcnt vmcnt(32)
	v_lshlrev_b32_e32 v18, 2, v84
	s_addc_u32 s17, s37, s17
	global_load_dwordx4 v[2:5], v18, s[18:19] offset:16
	global_load_dwordx4 v[6:9], v18, s[18:19]
	global_load_dwordx4 v[10:13], v18, s[16:17] offset:16
	global_load_dwordx4 v[14:17], v18, s[16:17]
	v_ashrrev_i32_e32 v19, 5, v50
	v_or_b32_e32 v25, 1, v19
	v_readlane_b32 s2, v255, 30
	v_readlane_b32 s6, v254, 23
	s_add_i32 s4, 0, 0x18000
	v_readlane_b32 s3, v255, 31
	v_add_u32_e32 v20, s6, v25
	v_and_b32_e32 v24, -2, v19
	v_add_u32_e32 v28, s4, v18
	v_lshl_add_u64 v[18:19], s[2:3], 0, v[98:99]
	v_ashrrev_i32_e32 v21, 31, v20
	v_readlane_b32 s2, v254, 15
	v_readlane_b32 s3, v255, 18
	v_lshlrev_b64 v[20:21], 11, v[20:21]
	v_and_b32_e32 v26, 63, v50
	s_add_u32 s2, s2, s3
	v_readlane_b32 s3, v254, 16
	v_lshlrev_b32_e32 v27, 11, v24
	v_lshlrev_b32_e32 v29, 11, v25
	v_lshl_or_b32 v20, v26, 4, v20
	s_addc_u32 s3, s3, 0
	v_lshl_add_u32 v22, v50, 1, 0
	v_lshl_add_u32 v23, v50, 2, s4
	v_lshl_add_u64 v[20:21], s[2:3], 0, v[20:21]
	v_add_u32_e32 v26, s6, v24
	s_mov_b32 s36, 0
	v_add_u32_e32 v27, v28, v27
	v_add_u32_e32 v28, v28, v29
	v_readlane_b32 s38, v251, 37
	v_readlane_b32 s39, v251, 38
	v_readlane_b32 s40, v251, 39
	v_readlane_b32 s41, v251, 40
	v_readlane_b32 s42, v251, 41
	v_readlane_b32 s43, v251, 42
	v_readlane_b32 s44, v251, 43
	v_readlane_b32 s45, v251, 44
	v_readlane_b32 s46, v251, 45
	v_readlane_b32 s47, v251, 46
	v_readlane_b32 s48, v251, 47
	v_readlane_b32 s49, v251, 48
	v_readlane_b32 s50, v251, 49
	v_readlane_b32 s51, v251, 50
	s_waitcnt lgkmcnt(0)
	s_barrier
	s_waitcnt vmcnt(0)
	v_mov_b32_e32 v110, v51
	v_mov_b32_e32 v111, v52
	v_mov_b32_e32 v112, v53
	v_mov_b32_e32 v113, v54
	v_mov_b32_e32 v114, v55
	v_mov_b32_e32 v115, v56
	v_mov_b32_e32 v116, v57
	v_mov_b32_e32 v117, v58
	v_mov_b32_e32 v118, v59
	v_mov_b32_e32 v119, v60
	v_mov_b32_e32 v120, v61
	v_mov_b32_e32 v121, v62
	v_mov_b32_e32 v122, v63
	v_mov_b32_e32 v123, v64
	v_mov_b32_e32 v124, v65
	v_mov_b32_e32 v125, v66
	v_mov_b32_e32 v126, v67
	v_mov_b32_e32 v127, v68
	v_mov_b32_e32 v128, v69
	v_mov_b32_e32 v129, v70
	v_mov_b32_e32 v130, v71
	v_mov_b32_e32 v131, v72
	v_mov_b32_e32 v132, v73
	v_mov_b32_e32 v133, v74
	v_mov_b32_e32 v134, v75
	v_mov_b32_e32 v135, v76
	v_mov_b32_e32 v136, v77
	v_mov_b32_e32 v137, v78
	v_mov_b32_e32 v138, v79
	v_mov_b32_e32 v139, v80
	v_mov_b32_e32 v140, v81
	v_mov_b32_e32 v141, v82
	v_mov_b32_e32 v142, v83
	s_branch .LBB0_2165

.LBB0_2165:
	ds_read_u16 v29, v22
	ds_read_u16 v30, v22 offset:1024
	ds_read_u16 v31, v22 offset:2048
	ds_read_u16 v32, v22 offset:3072
	ds_read_u16 v33, v22 offset:4096
	ds_read_u16 v34, v22 offset:5120
	ds_read_u16 v35, v22 offset:6144
	ds_read_u16 v36, v22 offset:7168
	s_waitcnt lgkmcnt(7)
	v_lshlrev_b32_e32 v29, 16, v29
	v_fma_f32 v29, v51, v29, v52
	s_waitcnt lgkmcnt(6)
	v_lshlrev_b32_e32 v30, 16, v30
	v_fmac_f32_e32 v29, v54, v30
	v_fma_f32 v30, v51, v30, v52
	s_waitcnt lgkmcnt(5)
	v_lshlrev_b32_e32 v31, 16, v31
	v_fmac_f32_e32 v29, v55, v31
	v_fmac_f32_e32 v30, v54, v31
	v_fma_f32 v31, v51, v31, v52
	s_waitcnt lgkmcnt(4)
	v_lshlrev_b32_e32 v32, 16, v32
	ds_read_u16 v37, v22 offset:8192
	ds_read_u16 v38, v22 offset:9216
	ds_read_u16 v39, v22 offset:10240
	ds_read_u16 v40, v22 offset:11264
	ds_read_u16 v41, v22 offset:12288
	ds_read_u16 v42, v22 offset:13312
	ds_read_u16 v43, v22 offset:14336
	ds_read_u16 v44, v22 offset:15360
	v_fmac_f32_e32 v29, v56, v32
	v_fmac_f32_e32 v30, v55, v32
	v_fmac_f32_e32 v31, v54, v32
	v_fma_f32 v32, v51, v32, v52
	s_waitcnt lgkmcnt(11)
	v_lshlrev_b32_e32 v33, 16, v33
	v_fmac_f32_e32 v29, v57, v33
	v_fmac_f32_e32 v30, v56, v33
	v_fmac_f32_e32 v31, v55, v33
	v_fmac_f32_e32 v32, v54, v33
	v_fma_f32 v33, v51, v33, v52
	s_waitcnt lgkmcnt(10)
	v_lshlrev_b32_e32 v34, 16, v34
	v_fmac_f32_e32 v29, v58, v34
	v_fmac_f32_e32 v30, v57, v34
	v_fmac_f32_e32 v31, v56, v34
	v_fmac_f32_e32 v32, v55, v34
	v_fmac_f32_e32 v33, v54, v34
	v_fma_f32 v34, v51, v34, v52
	s_waitcnt lgkmcnt(9)
	v_lshlrev_b32_e32 v35, 16, v35
	v_fmac_f32_e32 v29, v59, v35
	v_fmac_f32_e32 v30, v58, v35
	v_fmac_f32_e32 v31, v57, v35
	v_fmac_f32_e32 v32, v56, v35
	v_fmac_f32_e32 v33, v55, v35
	v_fmac_f32_e32 v34, v54, v35
	v_fma_f32 v35, v51, v35, v52
	s_waitcnt lgkmcnt(8)
	v_lshlrev_b32_e32 v36, 16, v36
	v_fmac_f32_e32 v29, v60, v36
	v_fmac_f32_e32 v30, v59, v36
	v_fmac_f32_e32 v31, v58, v36
	v_fmac_f32_e32 v32, v57, v36
	v_fmac_f32_e32 v33, v56, v36
	v_fmac_f32_e32 v34, v55, v36
	v_fmac_f32_e32 v35, v54, v36
	v_fma_f32 v36, v51, v36, v52
	s_waitcnt lgkmcnt(7)
	v_lshlrev_b32_e32 v37, 16, v37
	v_fmac_f32_e32 v29, v61, v37
	v_fmac_f32_e32 v30, v60, v37
	v_fmac_f32_e32 v31, v59, v37
	v_fmac_f32_e32 v32, v58, v37
	v_fmac_f32_e32 v33, v57, v37
	v_fmac_f32_e32 v34, v56, v37
	v_fmac_f32_e32 v35, v55, v37
	v_fmac_f32_e32 v36, v54, v37
	v_fma_f32 v37, v51, v37, v52
	s_waitcnt lgkmcnt(6)
	v_lshlrev_b32_e32 v38, 16, v38
	v_fmac_f32_e32 v29, v62, v38
	v_fmac_f32_e32 v30, v61, v38
	v_fmac_f32_e32 v31, v60, v38
	v_fmac_f32_e32 v32, v59, v38
	v_fmac_f32_e32 v33, v58, v38
	v_fmac_f32_e32 v34, v57, v38
	v_fmac_f32_e32 v35, v56, v38
	v_fmac_f32_e32 v36, v55, v38
	v_fmac_f32_e32 v37, v54, v38
	v_fma_f32 v38, v51, v38, v52
	s_waitcnt lgkmcnt(5)
	v_lshlrev_b32_e32 v39, 16, v39
	v_fmac_f32_e32 v29, v63, v39
	v_fmac_f32_e32 v30, v62, v39
	v_fmac_f32_e32 v31, v61, v39
	v_fmac_f32_e32 v32, v60, v39
	v_fmac_f32_e32 v33, v59, v39
	v_fmac_f32_e32 v34, v58, v39
	v_fmac_f32_e32 v35, v57, v39
	v_fmac_f32_e32 v36, v56, v39
	v_fmac_f32_e32 v37, v55, v39
	v_fmac_f32_e32 v38, v54, v39
	v_fma_f32 v39, v51, v39, v52
	s_waitcnt lgkmcnt(4)
	v_lshlrev_b32_e32 v40, 16, v40
	ds_read_u16 v45, v22 offset:16384
	v_fmac_f32_e32 v29, v64, v40
	v_fmac_f32_e32 v30, v63, v40
	v_fmac_f32_e32 v31, v62, v40
	v_fmac_f32_e32 v32, v61, v40
	v_fmac_f32_e32 v33, v60, v40
	v_fmac_f32_e32 v34, v59, v40
	v_fmac_f32_e32 v35, v58, v40
	v_fmac_f32_e32 v36, v57, v40
	v_fmac_f32_e32 v37, v56, v40
	v_fmac_f32_e32 v38, v55, v40
	v_fmac_f32_e32 v39, v54, v40
	v_fma_f32 v40, v51, v40, v52
	s_waitcnt lgkmcnt(4)
	v_lshlrev_b32_e32 v41, 16, v41
	v_fmac_f32_e32 v29, v65, v41
	v_fmac_f32_e32 v30, v64, v41
	v_fmac_f32_e32 v31, v63, v41
	v_fmac_f32_e32 v32, v62, v41
	v_fmac_f32_e32 v33, v61, v41
	v_fmac_f32_e32 v34, v60, v41
	v_fmac_f32_e32 v35, v59, v41
	v_fmac_f32_e32 v36, v58, v41
	v_fmac_f32_e32 v37, v57, v41
	v_fmac_f32_e32 v38, v56, v41
	v_fmac_f32_e32 v39, v55, v41
	v_fmac_f32_e32 v40, v54, v41
	v_fma_f32 v41, v51, v41, v52
	s_waitcnt lgkmcnt(3)
	v_lshlrev_b32_e32 v42, 16, v42
	v_fmac_f32_e32 v29, v66, v42
	v_fmac_f32_e32 v30, v65, v42
	v_fmac_f32_e32 v31, v64, v42
	v_fmac_f32_e32 v32, v63, v42
	v_fmac_f32_e32 v33, v62, v42
	v_fmac_f32_e32 v34, v61, v42
	v_fmac_f32_e32 v35, v60, v42
	v_fmac_f32_e32 v36, v59, v42
	v_fmac_f32_e32 v37, v58, v42
	v_fmac_f32_e32 v38, v57, v42
	v_fmac_f32_e32 v39, v56, v42
	v_fmac_f32_e32 v40, v55, v42
	v_fmac_f32_e32 v41, v54, v42
	v_fma_f32 v42, v51, v42, v52
	s_waitcnt lgkmcnt(2)
	v_lshlrev_b32_e32 v43, 16, v43
	v_fmac_f32_e32 v29, v67, v43
	v_fmac_f32_e32 v30, v66, v43
	v_fmac_f32_e32 v31, v65, v43
	v_fmac_f32_e32 v32, v64, v43
	v_fmac_f32_e32 v33, v63, v43
	v_fmac_f32_e32 v34, v62, v43
	v_fmac_f32_e32 v35, v61, v43
	v_fmac_f32_e32 v36, v60, v43
	v_fmac_f32_e32 v37, v59, v43
	v_fmac_f32_e32 v38, v58, v43
	v_fmac_f32_e32 v39, v57, v43
	v_fmac_f32_e32 v40, v56, v43
	v_fmac_f32_e32 v41, v55, v43
	v_fmac_f32_e32 v42, v54, v43
	v_fma_f32 v43, v51, v43, v52
	s_waitcnt lgkmcnt(1)
	v_lshlrev_b32_e32 v44, 16, v44
	v_fmac_f32_e32 v29, v68, v44
	v_fmac_f32_e32 v30, v67, v44
	v_fmac_f32_e32 v31, v66, v44
	v_fmac_f32_e32 v32, v65, v44
	v_fmac_f32_e32 v33, v64, v44
	v_fmac_f32_e32 v34, v63, v44
	v_fmac_f32_e32 v35, v62, v44
	v_fmac_f32_e32 v36, v61, v44
	v_fmac_f32_e32 v37, v60, v44
	v_fmac_f32_e32 v38, v59, v44
	v_fmac_f32_e32 v39, v58, v44
	v_fmac_f32_e32 v40, v57, v44
	v_fmac_f32_e32 v41, v56, v44
	v_fmac_f32_e32 v42, v55, v44
	v_fmac_f32_e32 v43, v54, v44
	v_fma_f32 v44, v51, v44, v52
	s_waitcnt lgkmcnt(0)
	v_lshlrev_b32_e32 v45, 16, v45
	v_fmac_f32_e32 v29, v69, v45
	v_fmac_f32_e32 v30, v68, v45
	v_fmac_f32_e32 v31, v67, v45
	v_fmac_f32_e32 v32, v66, v45
	v_fmac_f32_e32 v33, v65, v45
	v_fmac_f32_e32 v34, v64, v45
	v_fmac_f32_e32 v35, v63, v45
	v_fmac_f32_e32 v36, v62, v45
	v_fmac_f32_e32 v37, v61, v45
	v_fmac_f32_e32 v38, v60, v45
	v_fmac_f32_e32 v39, v59, v45
	v_fmac_f32_e32 v40, v58, v45
	v_fmac_f32_e32 v41, v57, v45
	v_fmac_f32_e32 v42, v56, v45
	v_fmac_f32_e32 v43, v55, v45
	v_fmac_f32_e32 v44, v54, v45
	ds_read_u16 v100, v22 offset:17408
	ds_read_u16 v101, v22 offset:18432
	ds_read_u16 v102, v22 offset:19456
	ds_read_u16 v103, v22 offset:20480
	ds_read_u16 v104, v22 offset:21504
	ds_read_u16 v105, v22 offset:22528
	ds_read_u16 v106, v22 offset:23552
	ds_read_u16 v107, v22 offset:24576
	s_waitcnt lgkmcnt(7)
	v_lshlrev_b32_e32 v108, 16, v100
	ds_read_u16 v100, v22 offset:25600
	v_fmac_f32_e32 v29, v70, v108
	v_pk_fma_f32 v[30:31], v[68:69], v[108:109], v[30:31] op_sel:[1,0,0] op_sel_hi:[0,0,1]
	v_pk_fma_f32 v[32:33], v[66:67], v[108:109], v[32:33] op_sel:[1,0,0] op_sel_hi:[0,0,1]
	v_pk_fma_f32 v[34:35], v[64:65], v[108:109], v[34:35] op_sel:[1,0,0] op_sel_hi:[0,0,1]
	v_pk_fma_f32 v[36:37], v[62:63], v[108:109], v[36:37] op_sel:[1,0,0] op_sel_hi:[0,0,1]
	v_pk_fma_f32 v[38:39], v[60:61], v[108:109], v[38:39] op_sel:[1,0,0] op_sel_hi:[0,0,1]
	v_pk_fma_f32 v[40:41], v[58:59], v[108:109], v[40:41] op_sel:[1,0,0] op_sel_hi:[0,0,1]
	v_pk_fma_f32 v[42:43], v[56:57], v[108:109], v[42:43] op_sel:[1,0,0] op_sel_hi:[0,0,1]
	v_fmac_f32_e32 v44, v55, v108
	s_waitcnt lgkmcnt(7)
	v_lshlrev_b32_e32 v108, 16, v101
	ds_read_u16 v101, v22 offset:26624
	v_fmac_f32_e32 v29, v71, v108
	v_pk_fma_f32 v[30:31], v[128:129], v[108:109], v[30:31] op_sel:[1,0,0] op_sel_hi:[0,0,1]
	v_pk_fma_f32 v[32:33], v[126:127], v[108:109], v[32:33] op_sel:[1,0,0] op_sel_hi:[0,0,1]
	v_pk_fma_f32 v[34:35], v[124:125], v[108:109], v[34:35] op_sel:[1,0,0] op_sel_hi:[0,0,1]
	v_pk_fma_f32 v[36:37], v[122:123], v[108:109], v[36:37] op_sel:[1,0,0] op_sel_hi:[0,0,1]
	v_pk_fma_f32 v[38:39], v[120:121], v[108:109], v[38:39] op_sel:[1,0,0] op_sel_hi:[0,0,1]
	v_pk_fma_f32 v[40:41], v[118:119], v[108:109], v[40:41] op_sel:[1,0,0] op_sel_hi:[0,0,1]
	v_pk_fma_f32 v[42:43], v[116:117], v[108:109], v[42:43] op_sel:[1,0,0] op_sel_hi:[0,0,1]
	v_fmac_f32_e32 v44, v56, v108
	s_waitcnt lgkmcnt(7)
	v_lshlrev_b32_e32 v108, 16, v102
	ds_read_u16 v102, v22 offset:27648
	v_fmac_f32_e32 v29, v72, v108
	v_pk_fma_f32 v[30:31], v[70:71], v[108:109], v[30:31] op_sel:[1,0,0] op_sel_hi:[0,0,1]
	v_pk_fma_f32 v[32:33], v[68:69], v[108:109], v[32:33] op_sel:[1,0,0] op_sel_hi:[0,0,1]
	v_pk_fma_f32 v[34:35], v[66:67], v[108:109], v[34:35] op_sel:[1,0,0] op_sel_hi:[0,0,1]
	v_pk_fma_f32 v[36:37], v[64:65], v[108:109], v[36:37] op_sel:[1,0,0] op_sel_hi:[0,0,1]
	v_pk_fma_f32 v[38:39], v[62:63], v[108:109], v[38:39] op_sel:[1,0,0] op_sel_hi:[0,0,1]
	v_pk_fma_f32 v[40:41], v[60:61], v[108:109], v[40:41] op_sel:[1,0,0] op_sel_hi:[0,0,1]
	v_pk_fma_f32 v[42:43], v[58:59], v[108:109], v[42:43] op_sel:[1,0,0] op_sel_hi:[0,0,1]
	v_fmac_f32_e32 v44, v57, v108
	s_waitcnt lgkmcnt(7)
	v_lshlrev_b32_e32 v108, 16, v103
	ds_read_u16 v103, v22 offset:28672
	v_fmac_f32_e32 v29, v73, v108
	v_pk_fma_f32 v[30:31], v[130:131], v[108:109], v[30:31] op_sel:[1,0,0] op_sel_hi:[0,0,1]
	v_pk_fma_f32 v[32:33], v[128:129], v[108:109], v[32:33] op_sel:[1,0,0] op_sel_hi:[0,0,1]
	v_pk_fma_f32 v[34:35], v[126:127], v[108:109], v[34:35] op_sel:[1,0,0] op_sel_hi:[0,0,1]
	v_pk_fma_f32 v[36:37], v[124:125], v[108:109], v[36:37] op_sel:[1,0,0] op_sel_hi:[0,0,1]
	v_pk_fma_f32 v[38:39], v[122:123], v[108:109], v[38:39] op_sel:[1,0,0] op_sel_hi:[0,0,1]
	v_pk_fma_f32 v[40:41], v[120:121], v[108:109], v[40:41] op_sel:[1,0,0] op_sel_hi:[0,0,1]
	v_pk_fma_f32 v[42:43], v[118:119], v[108:109], v[42:43] op_sel:[1,0,0] op_sel_hi:[0,0,1]
	v_fmac_f32_e32 v44, v58, v108
	s_waitcnt lgkmcnt(7)
	v_lshlrev_b32_e32 v108, 16, v104
	ds_read_u16 v104, v22 offset:29696
	v_fmac_f32_e32 v29, v74, v108
	v_pk_fma_f32 v[30:31], v[72:73], v[108:109], v[30:31] op_sel:[1,0,0] op_sel_hi:[0,0,1]
	v_pk_fma_f32 v[32:33], v[70:71], v[108:109], v[32:33] op_sel:[1,0,0] op_sel_hi:[0,0,1]
	v_pk_fma_f32 v[34:35], v[68:69], v[108:109], v[34:35] op_sel:[1,0,0] op_sel_hi:[0,0,1]
	v_pk_fma_f32 v[36:37], v[66:67], v[108:109], v[36:37] op_sel:[1,0,0] op_sel_hi:[0,0,1]
	v_pk_fma_f32 v[38:39], v[64:65], v[108:109], v[38:39] op_sel:[1,0,0] op_sel_hi:[0,0,1]
	v_pk_fma_f32 v[40:41], v[62:63], v[108:109], v[40:41] op_sel:[1,0,0] op_sel_hi:[0,0,1]
	v_pk_fma_f32 v[42:43], v[60:61], v[108:109], v[42:43] op_sel:[1,0,0] op_sel_hi:[0,0,1]
	v_fmac_f32_e32 v44, v59, v108
	s_waitcnt lgkmcnt(7)
	v_lshlrev_b32_e32 v108, 16, v105
	ds_read_u16 v105, v22 offset:30720
	v_fmac_f32_e32 v29, v75, v108
	v_pk_fma_f32 v[30:31], v[132:133], v[108:109], v[30:31] op_sel:[1,0,0] op_sel_hi:[0,0,1]
	v_pk_fma_f32 v[32:33], v[130:131], v[108:109], v[32:33] op_sel:[1,0,0] op_sel_hi:[0,0,1]
	v_pk_fma_f32 v[34:35], v[128:129], v[108:109], v[34:35] op_sel:[1,0,0] op_sel_hi:[0,0,1]
	v_pk_fma_f32 v[36:37], v[126:127], v[108:109], v[36:37] op_sel:[1,0,0] op_sel_hi:[0,0,1]
	v_pk_fma_f32 v[38:39], v[124:125], v[108:109], v[38:39] op_sel:[1,0,0] op_sel_hi:[0,0,1]
	v_pk_fma_f32 v[40:41], v[122:123], v[108:109], v[40:41] op_sel:[1,0,0] op_sel_hi:[0,0,1]
	v_pk_fma_f32 v[42:43], v[120:121], v[108:109], v[42:43] op_sel:[1,0,0] op_sel_hi:[0,0,1]
	v_fmac_f32_e32 v44, v60, v108
	s_waitcnt lgkmcnt(7)
	v_lshlrev_b32_e32 v108, 16, v106
	ds_read_u16 v106, v22 offset:31744
	v_fmac_f32_e32 v29, v76, v108
	v_pk_fma_f32 v[30:31], v[74:75], v[108:109], v[30:31] op_sel:[1,0,0] op_sel_hi:[0,0,1]
	v_pk_fma_f32 v[32:33], v[72:73], v[108:109], v[32:33] op_sel:[1,0,0] op_sel_hi:[0,0,1]
	v_pk_fma_f32 v[34:35], v[70:71], v[108:109], v[34:35] op_sel:[1,0,0] op_sel_hi:[0,0,1]
	v_pk_fma_f32 v[36:37], v[68:69], v[108:109], v[36:37] op_sel:[1,0,0] op_sel_hi:[0,0,1]
	v_pk_fma_f32 v[38:39], v[66:67], v[108:109], v[38:39] op_sel:[1,0,0] op_sel_hi:[0,0,1]
	v_pk_fma_f32 v[40:41], v[64:65], v[108:109], v[40:41] op_sel:[1,0,0] op_sel_hi:[0,0,1]
	v_pk_fma_f32 v[42:43], v[62:63], v[108:109], v[42:43] op_sel:[1,0,0] op_sel_hi:[0,0,1]
	v_fmac_f32_e32 v44, v61, v108
	s_waitcnt lgkmcnt(7)
	v_lshlrev_b32_e32 v108, 16, v107
	ds_read_u16 v107, v22 offset:32768
	v_fmac_f32_e32 v29, v77, v108
	v_pk_fma_f32 v[30:31], v[134:135], v[108:109], v[30:31] op_sel:[1,0,0] op_sel_hi:[0,0,1]
	v_pk_fma_f32 v[32:33], v[132:133], v[108:109], v[32:33] op_sel:[1,0,0] op_sel_hi:[0,0,1]
	v_pk_fma_f32 v[34:35], v[130:131], v[108:109], v[34:35] op_sel:[1,0,0] op_sel_hi:[0,0,1]
	v_pk_fma_f32 v[36:37], v[128:129], v[108:109], v[36:37] op_sel:[1,0,0] op_sel_hi:[0,0,1]
	v_pk_fma_f32 v[38:39], v[126:127], v[108:109], v[38:39] op_sel:[1,0,0] op_sel_hi:[0,0,1]
	v_pk_fma_f32 v[40:41], v[124:125], v[108:109], v[40:41] op_sel:[1,0,0] op_sel_hi:[0,0,1]
	v_pk_fma_f32 v[42:43], v[122:123], v[108:109], v[42:43] op_sel:[1,0,0] op_sel_hi:[0,0,1]
	v_fmac_f32_e32 v44, v62, v108
	s_waitcnt lgkmcnt(7)
	v_lshlrev_b32_e32 v108, 16, v100
	ds_read_u16 v100, v22 offset:33792
	v_fmac_f32_e32 v29, v78, v108
	v_pk_fma_f32 v[30:31], v[76:77], v[108:109], v[30:31] op_sel:[1,0,0] op_sel_hi:[0,0,1]
	v_pk_fma_f32 v[32:33], v[74:75], v[108:109], v[32:33] op_sel:[1,0,0] op_sel_hi:[0,0,1]
	v_pk_fma_f32 v[34:35], v[72:73], v[108:109], v[34:35] op_sel:[1,0,0] op_sel_hi:[0,0,1]
	v_pk_fma_f32 v[36:37], v[70:71], v[108:109], v[36:37] op_sel:[1,0,0] op_sel_hi:[0,0,1]
	v_pk_fma_f32 v[38:39], v[68:69], v[108:109], v[38:39] op_sel:[1,0,0] op_sel_hi:[0,0,1]
	v_pk_fma_f32 v[40:41], v[66:67], v[108:109], v[40:41] op_sel:[1,0,0] op_sel_hi:[0,0,1]
	v_pk_fma_f32 v[42:43], v[64:65], v[108:109], v[42:43] op_sel:[1,0,0] op_sel_hi:[0,0,1]
	v_fmac_f32_e32 v44, v63, v108
	s_waitcnt lgkmcnt(7)
	v_lshlrev_b32_e32 v108, 16, v101
	ds_read_u16 v101, v22 offset:34816
	v_fmac_f32_e32 v29, v79, v108
	v_pk_fma_f32 v[30:31], v[136:137], v[108:109], v[30:31] op_sel:[1,0,0] op_sel_hi:[0,0,1]
	v_pk_fma_f32 v[32:33], v[134:135], v[108:109], v[32:33] op_sel:[1,0,0] op_sel_hi:[0,0,1]
	v_pk_fma_f32 v[34:35], v[132:133], v[108:109], v[34:35] op_sel:[1,0,0] op_sel_hi:[0,0,1]
	v_pk_fma_f32 v[36:37], v[130:131], v[108:109], v[36:37] op_sel:[1,0,0] op_sel_hi:[0,0,1]
	v_pk_fma_f32 v[38:39], v[128:129], v[108:109], v[38:39] op_sel:[1,0,0] op_sel_hi:[0,0,1]
	v_pk_fma_f32 v[40:41], v[126:127], v[108:109], v[40:41] op_sel:[1,0,0] op_sel_hi:[0,0,1]
	v_pk_fma_f32 v[42:43], v[124:125], v[108:109], v[42:43] op_sel:[1,0,0] op_sel_hi:[0,0,1]
	v_fmac_f32_e32 v44, v64, v108
	s_waitcnt lgkmcnt(7)
	v_lshlrev_b32_e32 v108, 16, v102
	ds_read_u16 v102, v22 offset:35840
	v_fmac_f32_e32 v29, v80, v108
	v_pk_fma_f32 v[30:31], v[78:79], v[108:109], v[30:31] op_sel:[1,0,0] op_sel_hi:[0,0,1]
	v_pk_fma_f32 v[32:33], v[76:77], v[108:109], v[32:33] op_sel:[1,0,0] op_sel_hi:[0,0,1]
	v_pk_fma_f32 v[34:35], v[74:75], v[108:109], v[34:35] op_sel:[1,0,0] op_sel_hi:[0,0,1]
	v_pk_fma_f32 v[36:37], v[72:73], v[108:109], v[36:37] op_sel:[1,0,0] op_sel_hi:[0,0,1]
	v_pk_fma_f32 v[38:39], v[70:71], v[108:109], v[38:39] op_sel:[1,0,0] op_sel_hi:[0,0,1]
	v_pk_fma_f32 v[40:41], v[68:69], v[108:109], v[40:41] op_sel:[1,0,0] op_sel_hi:[0,0,1]
	v_pk_fma_f32 v[42:43], v[66:67], v[108:109], v[42:43] op_sel:[1,0,0] op_sel_hi:[0,0,1]
	v_fmac_f32_e32 v44, v65, v108
	s_waitcnt lgkmcnt(7)
	v_lshlrev_b32_e32 v108, 16, v103
	ds_read_u16 v103, v22 offset:36864
	v_fmac_f32_e32 v29, v81, v108
	v_pk_fma_f32 v[30:31], v[138:139], v[108:109], v[30:31] op_sel:[1,0,0] op_sel_hi:[0,0,1]
	v_pk_fma_f32 v[32:33], v[136:137], v[108:109], v[32:33] op_sel:[1,0,0] op_sel_hi:[0,0,1]
	v_pk_fma_f32 v[34:35], v[134:135], v[108:109], v[34:35] op_sel:[1,0,0] op_sel_hi:[0,0,1]
	v_pk_fma_f32 v[36:37], v[132:133], v[108:109], v[36:37] op_sel:[1,0,0] op_sel_hi:[0,0,1]
	v_pk_fma_f32 v[38:39], v[130:131], v[108:109], v[38:39] op_sel:[1,0,0] op_sel_hi:[0,0,1]
	v_pk_fma_f32 v[40:41], v[128:129], v[108:109], v[40:41] op_sel:[1,0,0] op_sel_hi:[0,0,1]
	v_pk_fma_f32 v[42:43], v[126:127], v[108:109], v[42:43] op_sel:[1,0,0] op_sel_hi:[0,0,1]
	v_fmac_f32_e32 v44, v66, v108
	s_waitcnt lgkmcnt(7)
	v_lshlrev_b32_e32 v108, 16, v104
	ds_read_u16 v104, v22 offset:37888
	v_fmac_f32_e32 v29, v82, v108
	v_pk_fma_f32 v[30:31], v[80:81], v[108:109], v[30:31] op_sel:[1,0,0] op_sel_hi:[0,0,1]
	v_pk_fma_f32 v[32:33], v[78:79], v[108:109], v[32:33] op_sel:[1,0,0] op_sel_hi:[0,0,1]
	v_pk_fma_f32 v[34:35], v[76:77], v[108:109], v[34:35] op_sel:[1,0,0] op_sel_hi:[0,0,1]
	v_pk_fma_f32 v[36:37], v[74:75], v[108:109], v[36:37] op_sel:[1,0,0] op_sel_hi:[0,0,1]
	v_pk_fma_f32 v[38:39], v[72:73], v[108:109], v[38:39] op_sel:[1,0,0] op_sel_hi:[0,0,1]
	v_pk_fma_f32 v[40:41], v[70:71], v[108:109], v[40:41] op_sel:[1,0,0] op_sel_hi:[0,0,1]
	v_pk_fma_f32 v[42:43], v[68:69], v[108:109], v[42:43] op_sel:[1,0,0] op_sel_hi:[0,0,1]
	v_fmac_f32_e32 v44, v67, v108
	s_waitcnt lgkmcnt(7)
	v_lshlrev_b32_e32 v108, 16, v105
	ds_read_u16 v105, v22 offset:38912
	v_fmac_f32_e32 v29, v83, v108
	v_pk_fma_f32 v[30:31], v[140:141], v[108:109], v[30:31] op_sel:[1,0,0] op_sel_hi:[0,0,1]
	v_pk_fma_f32 v[32:33], v[138:139], v[108:109], v[32:33] op_sel:[1,0,0] op_sel_hi:[0,0,1]
	v_pk_fma_f32 v[34:35], v[136:137], v[108:109], v[34:35] op_sel:[1,0,0] op_sel_hi:[0,0,1]
	v_pk_fma_f32 v[36:37], v[134:135], v[108:109], v[36:37] op_sel:[1,0,0] op_sel_hi:[0,0,1]
	v_pk_fma_f32 v[38:39], v[132:133], v[108:109], v[38:39] op_sel:[1,0,0] op_sel_hi:[0,0,1]
	v_pk_fma_f32 v[40:41], v[130:131], v[108:109], v[40:41] op_sel:[1,0,0] op_sel_hi:[0,0,1]
	v_pk_fma_f32 v[42:43], v[128:129], v[108:109], v[42:43] op_sel:[1,0,0] op_sel_hi:[0,0,1]
	v_fmac_f32_e32 v44, v68, v108
	s_waitcnt lgkmcnt(7)
	v_lshlrev_b32_e32 v108, 16, v106
	ds_read_u16 v106, v22 offset:39936
	v_pk_fma_f32 v[30:31], v[82:83], v[108:109], v[30:31] op_sel:[1,0,0] op_sel_hi:[0,0,1]
	v_pk_fma_f32 v[32:33], v[80:81], v[108:109], v[32:33] op_sel:[1,0,0] op_sel_hi:[0,0,1]
	v_pk_fma_f32 v[34:35], v[78:79], v[108:109], v[34:35] op_sel:[1,0,0] op_sel_hi:[0,0,1]
	v_pk_fma_f32 v[36:37], v[76:77], v[108:109], v[36:37] op_sel:[1,0,0] op_sel_hi:[0,0,1]
	v_pk_fma_f32 v[38:39], v[74:75], v[108:109], v[38:39] op_sel:[1,0,0] op_sel_hi:[0,0,1]
	v_pk_fma_f32 v[40:41], v[72:73], v[108:109], v[40:41] op_sel:[1,0,0] op_sel_hi:[0,0,1]
	v_pk_fma_f32 v[42:43], v[70:71], v[108:109], v[42:43] op_sel:[1,0,0] op_sel_hi:[0,0,1]
	v_fmac_f32_e32 v44, v69, v108
	s_waitcnt lgkmcnt(7)
	v_lshlrev_b32_e32 v108, 16, v107
	ds_read_u16 v107, v22 offset:40960
	v_fmac_f32_e32 v31, v83, v108
	v_pk_fma_f32 v[32:33], v[140:141], v[108:109], v[32:33] op_sel:[1,0,0] op_sel_hi:[0,0,1]
	v_pk_fma_f32 v[34:35], v[138:139], v[108:109], v[34:35] op_sel:[1,0,0] op_sel_hi:[0,0,1]
	v_pk_fma_f32 v[36:37], v[136:137], v[108:109], v[36:37] op_sel:[1,0,0] op_sel_hi:[0,0,1]
	v_pk_fma_f32 v[38:39], v[134:135], v[108:109], v[38:39] op_sel:[1,0,0] op_sel_hi:[0,0,1]
	v_pk_fma_f32 v[40:41], v[132:133], v[108:109], v[40:41] op_sel:[1,0,0] op_sel_hi:[0,0,1]
	v_pk_fma_f32 v[42:43], v[130:131], v[108:109], v[42:43] op_sel:[1,0,0] op_sel_hi:[0,0,1]
	v_fmac_f32_e32 v44, v70, v108
	s_waitcnt lgkmcnt(7)
	v_lshlrev_b32_e32 v108, 16, v100
	ds_read_u16 v100, v22 offset:41984
	v_pk_fma_f32 v[32:33], v[82:83], v[108:109], v[32:33] op_sel:[1,0,0] op_sel_hi:[0,0,1]
	v_pk_fma_f32 v[34:35], v[80:81], v[108:109], v[34:35] op_sel:[1,0,0] op_sel_hi:[0,0,1]
	v_pk_fma_f32 v[36:37], v[78:79], v[108:109], v[36:37] op_sel:[1,0,0] op_sel_hi:[0,0,1]
	v_pk_fma_f32 v[38:39], v[76:77], v[108:109], v[38:39] op_sel:[1,0,0] op_sel_hi:[0,0,1]
	v_pk_fma_f32 v[40:41], v[74:75], v[108:109], v[40:41] op_sel:[1,0,0] op_sel_hi:[0,0,1]
	v_pk_fma_f32 v[42:43], v[72:73], v[108:109], v[42:43] op_sel:[1,0,0] op_sel_hi:[0,0,1]
	v_fmac_f32_e32 v44, v71, v108
	s_waitcnt lgkmcnt(7)
	v_lshlrev_b32_e32 v108, 16, v101
	ds_read_u16 v101, v22 offset:43008
	v_fmac_f32_e32 v33, v83, v108
	v_pk_fma_f32 v[34:35], v[140:141], v[108:109], v[34:35] op_sel:[1,0,0] op_sel_hi:[0,0,1]
	v_pk_fma_f32 v[36:37], v[138:139], v[108:109], v[36:37] op_sel:[1,0,0] op_sel_hi:[0,0,1]
	v_pk_fma_f32 v[38:39], v[136:137], v[108:109], v[38:39] op_sel:[1,0,0] op_sel_hi:[0,0,1]
	v_pk_fma_f32 v[40:41], v[134:135], v[108:109], v[40:41] op_sel:[1,0,0] op_sel_hi:[0,0,1]
	v_pk_fma_f32 v[42:43], v[132:133], v[108:109], v[42:43] op_sel:[1,0,0] op_sel_hi:[0,0,1]
	v_fmac_f32_e32 v44, v72, v108
	s_waitcnt lgkmcnt(7)
	v_lshlrev_b32_e32 v108, 16, v102
	ds_read_u16 v102, v22 offset:44032
	v_pk_fma_f32 v[34:35], v[82:83], v[108:109], v[34:35] op_sel:[1,0,0] op_sel_hi:[0,0,1]
	v_pk_fma_f32 v[36:37], v[80:81], v[108:109], v[36:37] op_sel:[1,0,0] op_sel_hi:[0,0,1]
	v_pk_fma_f32 v[38:39], v[78:79], v[108:109], v[38:39] op_sel:[1,0,0] op_sel_hi:[0,0,1]
	v_pk_fma_f32 v[40:41], v[76:77], v[108:109], v[40:41] op_sel:[1,0,0] op_sel_hi:[0,0,1]
	v_pk_fma_f32 v[42:43], v[74:75], v[108:109], v[42:43] op_sel:[1,0,0] op_sel_hi:[0,0,1]
	v_fmac_f32_e32 v44, v73, v108
	s_waitcnt lgkmcnt(7)
	v_lshlrev_b32_e32 v108, 16, v103
	ds_read_u16 v103, v22 offset:45056
	v_fmac_f32_e32 v35, v83, v108
	v_pk_fma_f32 v[36:37], v[140:141], v[108:109], v[36:37] op_sel:[1,0,0] op_sel_hi:[0,0,1]
	v_pk_fma_f32 v[38:39], v[138:139], v[108:109], v[38:39] op_sel:[1,0,0] op_sel_hi:[0,0,1]
	v_pk_fma_f32 v[40:41], v[136:137], v[108:109], v[40:41] op_sel:[1,0,0] op_sel_hi:[0,0,1]
	v_pk_fma_f32 v[42:43], v[134:135], v[108:109], v[42:43] op_sel:[1,0,0] op_sel_hi:[0,0,1]
	v_fmac_f32_e32 v44, v74, v108
	s_waitcnt lgkmcnt(7)
	v_lshlrev_b32_e32 v108, 16, v104
	ds_read_u16 v104, v22 offset:46080
	v_pk_fma_f32 v[36:37], v[82:83], v[108:109], v[36:37] op_sel:[1,0,0] op_sel_hi:[0,0,1]
	v_pk_fma_f32 v[38:39], v[80:81], v[108:109], v[38:39] op_sel:[1,0,0] op_sel_hi:[0,0,1]
	v_pk_fma_f32 v[40:41], v[78:79], v[108:109], v[40:41] op_sel:[1,0,0] op_sel_hi:[0,0,1]
	v_pk_fma_f32 v[42:43], v[76:77], v[108:109], v[42:43] op_sel:[1,0,0] op_sel_hi:[0,0,1]
	v_fmac_f32_e32 v44, v75, v108
	s_waitcnt lgkmcnt(7)
	v_lshlrev_b32_e32 v108, 16, v105
	v_fmac_f32_e32 v37, v83, v108
	v_pk_fma_f32 v[38:39], v[140:141], v[108:109], v[38:39] op_sel:[1,0,0] op_sel_hi:[0,0,1]
	v_pk_fma_f32 v[40:41], v[138:139], v[108:109], v[40:41] op_sel:[1,0,0] op_sel_hi:[0,0,1]
	v_pk_fma_f32 v[42:43], v[136:137], v[108:109], v[42:43] op_sel:[1,0,0] op_sel_hi:[0,0,1]
	v_fmac_f32_e32 v44, v76, v108
	s_waitcnt lgkmcnt(6)
	v_lshlrev_b32_e32 v108, 16, v106
	v_pk_fma_f32 v[38:39], v[82:83], v[108:109], v[38:39] op_sel:[1,0,0] op_sel_hi:[0,0,1]
	v_pk_fma_f32 v[40:41], v[80:81], v[108:109], v[40:41] op_sel:[1,0,0] op_sel_hi:[0,0,1]
	v_pk_fma_f32 v[42:43], v[78:79], v[108:109], v[42:43] op_sel:[1,0,0] op_sel_hi:[0,0,1]
	v_fmac_f32_e32 v44, v77, v108
	s_waitcnt lgkmcnt(5)
	v_lshlrev_b32_e32 v108, 16, v107
	v_fmac_f32_e32 v39, v83, v108
	v_pk_fma_f32 v[40:41], v[140:141], v[108:109], v[40:41] op_sel:[1,0,0] op_sel_hi:[0,0,1]
	v_pk_fma_f32 v[42:43], v[138:139], v[108:109], v[42:43] op_sel:[1,0,0] op_sel_hi:[0,0,1]
	v_fmac_f32_e32 v44, v78, v108
	s_waitcnt lgkmcnt(4)
	v_lshlrev_b32_e32 v108, 16, v100
	v_pk_fma_f32 v[40:41], v[82:83], v[108:109], v[40:41] op_sel:[1,0,0] op_sel_hi:[0,0,1]
	v_pk_fma_f32 v[42:43], v[80:81], v[108:109], v[42:43] op_sel:[1,0,0] op_sel_hi:[0,0,1]
	v_fmac_f32_e32 v44, v79, v108
	s_waitcnt lgkmcnt(3)
	v_lshlrev_b32_e32 v108, 16, v101
	v_fmac_f32_e32 v41, v83, v108
	v_pk_fma_f32 v[42:43], v[140:141], v[108:109], v[42:43] op_sel:[1,0,0] op_sel_hi:[0,0,1]
	v_fmac_f32_e32 v44, v80, v108
	s_waitcnt lgkmcnt(2)
	v_lshlrev_b32_e32 v108, 16, v102
	v_pk_fma_f32 v[42:43], v[82:83], v[108:109], v[42:43] op_sel:[1,0,0] op_sel_hi:[0,0,1]
	v_fmac_f32_e32 v44, v81, v108
	s_waitcnt lgkmcnt(1)
	v_lshlrev_b32_e32 v108, 16, v103
	v_fmac_f32_e32 v43, v83, v108
	v_fmac_f32_e32 v44, v82, v108
	s_waitcnt lgkmcnt(0)
	v_lshlrev_b32_e32 v108, 16, v104
	v_fmac_f32_e32 v44, v83, v108
	ds_write2st64_b32 v23, v29, v30 offset1:8
	ds_write2st64_b32 v23, v31, v32 offset0:16 offset1:24
	ds_write2st64_b32 v23, v33, v34 offset0:32 offset1:40
	ds_write2st64_b32 v23, v35, v36 offset0:48 offset1:56
	ds_write2st64_b32 v23, v37, v38 offset0:64 offset1:72
	ds_write2st64_b32 v23, v39, v40 offset0:80 offset1:88
	ds_write2st64_b32 v23, v41, v42 offset0:96 offset1:104
	ds_write2st64_b32 v23, v43, v44 offset0:112 offset1:120
	v_add_u32_e32 v29, s36, v24
	v_cmp_gt_i32_e32 vcc, 64, v29
	s_waitcnt lgkmcnt(0)
	s_barrier
	s_and_saveexec_b64 s[34:35], vcc
	s_cbranch_execz .LBB0_2167
	ds_read_b128 v[30:33], v27
	ds_read_b128 v[34:37], v27 offset:16
	s_waitcnt lgkmcnt(1)
	v_mov_b32_e32 v38, v31
	v_mov_b32_e32 v39, v32
	v_mov_b32_e32 v40, v30
	v_mov_b32_e32 v41, v33
	v_pk_add_f32 v[38:39], v[38:39], v[40:41]
	s_waitcnt lgkmcnt(0)
	v_mov_b32_e32 v40, v36
	v_mov_b32_e32 v41, v34
	v_mov_b32_e32 v42, v37
	v_mov_b32_e32 v43, v35
	v_pk_add_f32 v[40:41], v[40:41], v[42:43]
	v_add_f32_e32 v29, v38, v39
	v_add_f32_e32 v29, v29, v41
	v_add_f32_e32 v29, v40, v29
	v_and_b32_e32 v39, 64, v214
	v_xor_b32_e32 v38, 16, v214
	v_add_f32_dpp v29, v29, v29 quad_perm:[1,0,3,2] row_mask:0xf bank_mask:0xf bound_ctrl:1
	v_add_u32_e32 v39, 64, v39
	v_cmp_lt_i32_e32 vcc, v38, v39
	v_add_f32_dpp v29, v29, v29 quad_perm:[2,3,0,1] row_mask:0xf bank_mask:0xf bound_ctrl:1
	s_nop 0
	v_cndmask_b32_e32 v38, v214, v38, vcc
	v_add_f32_dpp v29, v29, v29 row_half_mirror row_mask:0xf bank_mask:0xf bound_ctrl:1
	v_lshlrev_b32_e32 v46, 2, v38
	s_nop 0
	v_add_f32_dpp v29, v29, v29 row_mirror row_mask:0xf bank_mask:0xf bound_ctrl:1
	ds_bpermute_b32 v38, v46, v29
	s_waitcnt lgkmcnt(0)
	v_add_f32_e32 v29, v29, v38
	v_xor_b32_e32 v38, 32, v214
	v_cmp_lt_i32_e32 vcc, v38, v39
	s_nop 1
	v_cndmask_b32_e32 v38, v214, v38, vcc
	v_lshlrev_b32_e32 v47, 2, v38
	ds_bpermute_b32 v38, v47, v29
	s_waitcnt lgkmcnt(0)
	v_add_f32_e32 v29, v29, v38
	v_fmamk_f32 v31, v29, 0xbb000000, v31
	v_fmamk_f32 v30, v29, 0xbb000000, v30
	v_fmamk_f32 v33, v29, 0xbb000000, v33
	v_fmac_f32_e32 v32, 0xbb000000, v29
	v_pk_mul_f32 v[38:39], v[32:33], v[32:33]
	v_pk_mul_f32 v[40:41], v[30:31], v[30:31]
	v_fmamk_f32 v35, v29, 0xbb000000, v35
	v_fmamk_f32 v34, v29, 0xbb000000, v34
	v_fmamk_f32 v37, v29, 0xbb000000, v37
	v_fmac_f32_e32 v36, 0xbb000000, v29
	v_pk_mov_b32 v[42:43], v[40:41], v[38:39] op_sel:[1,0]
	v_mov_b32_e32 v41, v39
	v_pk_add_f32 v[38:39], v[42:43], v[40:41]
	v_pk_mul_f32 v[40:41], v[36:37], v[36:37]
	v_pk_mul_f32 v[42:43], v[34:35], v[34:35]
	v_mov_b32_e32 v44, v40
	v_mov_b32_e32 v45, v42
	v_mov_b32_e32 v42, v41
	v_pk_add_f32 v[40:41], v[44:45], v[42:43]
	v_add_f32_e32 v29, v38, v39
	v_add_f32_e32 v29, v41, v29
	v_add_f32_e32 v29, v40, v29
	s_nop 1
	v_add_f32_dpp v29, v29, v29 quad_perm:[1,0,3,2] row_mask:0xf bank_mask:0xf bound_ctrl:1
	s_nop 1
	v_add_f32_dpp v29, v29, v29 quad_perm:[2,3,0,1] row_mask:0xf bank_mask:0xf bound_ctrl:1
	s_nop 1
	v_add_f32_dpp v29, v29, v29 row_half_mirror row_mask:0xf bank_mask:0xf bound_ctrl:1
	s_nop 1
	v_add_f32_dpp v29, v29, v29 row_mirror row_mask:0xf bank_mask:0xf bound_ctrl:1
	ds_bpermute_b32 v38, v46, v29
	s_waitcnt lgkmcnt(0)
	v_add_f32_e32 v29, v29, v38
	ds_bpermute_b32 v38, v47, v29
	s_waitcnt lgkmcnt(0)
	v_add_f32_e32 v29, v29, v38
	v_fmamk_f32 v29, v29, 0x3b000000, v1
	v_mul_f32_e32 v38, 0x4b800000, v29
	v_cmp_gt_f32_e32 vcc, s77, v29
	s_nop 1
	v_cndmask_b32_e32 v29, v29, v38, vcc
	v_rsq_f32_e32 v29, v29
	s_nop 0
	v_mul_f32_e32 v38, 0x45800000, v29
	v_cndmask_b32_e32 v38, v29, v38, vcc
	v_pk_mul_f32 v[30:31], v[30:31], v[38:39] op_sel_hi:[1,0]
	v_pk_mul_f32 v[34:35], v[34:35], v[38:39] op_sel_hi:[1,0]
	v_pk_fma_f32 v[30:31], v[6:7], v[30:31], v[14:15]
	v_pk_fma_f32 v[34:35], v[2:3], v[34:35], v[10:11]
	v_mul_f32_e32 v29, 0xbfb8aa3b, v30
	v_pk_mul_f32 v[32:33], v[32:33], v[38:39] op_sel_hi:[1,0]
	v_pk_mul_f32 v[36:37], v[36:37], v[38:39] op_sel_hi:[1,0]
	v_exp_f32_e32 v29, v29
	v_mul_f32_e32 v38, 0xbfb8aa3b, v34
	v_exp_f32_e32 v39, v38
	v_mul_f32_e32 v40, 0xbfb8aa3b, v35
	v_add_f32_e32 v29, 1.0, v29
	v_rcp_f32_e32 v38, v29
	v_add_f32_e32 v29, 1.0, v39
	v_mul_f32_e32 v39, 0xbfb8aa3b, v31
	v_exp_f32_e32 v39, v39
	v_exp_f32_e32 v41, v40
	v_pk_fma_f32 v[32:33], v[8:9], v[32:33], v[16:17]
	v_rcp_f32_e32 v40, v29
	v_add_f32_e32 v29, 1.0, v39
	v_pk_fma_f32 v[36:37], v[4:5], v[36:37], v[12:13]
	v_rcp_f32_e32 v39, v29
	v_add_f32_e32 v29, 1.0, v41
	v_mul_f32_e32 v41, 0xbfb8aa3b, v32
	v_exp_f32_e32 v42, v41
	v_mul_f32_e32 v41, 0xbfb8aa3b, v36
	v_exp_f32_e32 v43, v41
	v_rcp_f32_e32 v41, v29
	v_add_f32_e32 v29, 1.0, v42
	v_rcp_f32_e32 v42, v29
	v_add_f32_e32 v29, 1.0, v43
	v_mul_f32_e32 v43, 0xbfb8aa3b, v33
	v_exp_f32_e32 v43, v43
	v_mul_f32_e32 v44, 0xbfb8aa3b, v37
	v_exp_f32_e32 v45, v44
	v_rcp_f32_e32 v44, v29
	v_add_f32_e32 v29, 1.0, v43
	v_rcp_f32_e32 v43, v29
	v_add_f32_e32 v29, 1.0, v45
	v_rcp_f32_e32 v45, v29
	v_pk_mul_f32 v[30:31], v[30:31], v[38:39]
	v_pk_mul_f32 v[34:35], v[34:35], v[40:41]
	v_pk_mul_f32 v[32:33], v[32:33], v[42:43]
	v_cvt_pk_bf16_f32 v30, v30, v31
	v_cvt_pk_bf16_f32 v31, v32, v33
	v_cvt_pk_bf16_f32 v32, v34, v35
	v_add_u32_e32 v34, s36, v26
	v_ashrrev_i32_e32 v35, 31, v34
	v_pk_mul_f32 v[36:37], v[36:37], v[44:45]
	v_lshlrev_b64 v[34:35], 11, v[34:35]
	v_cvt_pk_bf16_f32 v33, v36, v37
	v_lshl_add_u64 v[34:35], v[18:19], 0, v[34:35]
	global_store_dwordx4 v[34:35], v[30:33], off offset:1024
